# expert-up epilogue: hoist 8 row-rstd loads, counted vmcnt
# baseline (speedup 1.0000x reference)
; __device__ __forceinline__ float sigm(float x) { return __builtin_amdgcn_rcpf(1.f + __builtin_amdgcn_exp2f(-1.4426950408889634f * x)); }
; __device__ __forceinline__ unsigned pk4_fp8(float a, float b, float c, float d) { int w = 0; w = __builtin_amdgcn_cvt_pk_fp8_f32(a, b, w, false); w = __builtin_amdgcn_cvt_pk_fp8_f32(c, d, w, true); return (unsigned)w; }
; __device__ __forceinline__ u32x4 pack8(f32x4 v0, f32x4 v1) { u32x4 w; w.x = cvt_pk_bf16(v0[0], v0[1]); w.y = cvt_pk_bf16(v0[2], v0[3]); w.z = cvt_pk_bf16(v1[0], v1[1]); w.w = cvt_pk_bf16(v1[2], v1[3]); return w; }
; template <class T> __device__ __forceinline__ void est(T* p, T v) { if constexpr (MK_EPI_NT != 0) __builtin_nontemporal_store(v, p); else *p = v; }
; __device__ __forceinline__ float ss_val(const ss_t* ss, int row) { return (float)ss[row] * (1.f / 16777216.f); }
;     __device__ __forceinline__ void operator()(AccT acc, const Unit& u, int wr, int wc, int fr, int fq) const {
;         const int row0 = u.pm * 256 + wr * 64 + fr, col0 = u.pn * 128 + wc * 32 + 8 * fq;
; #pragma unroll
;         for (int ai = 0; ai < 2; ++ai)
; #pragma unroll
;             for (int m = 0; m < 4; ++m) { const int row = row0 + ai * 128 + m * 16; const float r = (is_rstd ? ((const float*)rs)[row] : rsqrtf(ss_val((const ss_t*)rs, row) * (1.0f / DM) + EPS)) * ascale;
;                 f32x4 o[2];
; #pragma unroll
;                 for (int bj = 0; bj < 2; ++bj) { const f32x4 a = acc[ai][bj][m][0] * r, b = acc[ai][bj][m][1] * r;
; #pragma unroll
;                     for (int j = 0; j < 4; ++j) o[bj][j] = a[j] * sigm(a[j]) * b[j]; }
;                 if constexpr (F8OUT) est((u32x2*)((unsigned char*)O + (size_t)row * ldo + col0), (u32x2)(u32x2){pk4_fp8(o[0][0], o[0][1], o[0][2], o[0][3]), pk4_fp8(o[1][0], o[1][1], o[1][2], o[1][3])});
;                 else est((u32x4*)((bf16_t*)O + (size_t)row * ldo + col0), (u32x4)pack8(o[0], o[1])); }
;     }
.LBB0_2262:
	v_lshl_add_u32 v2, s62, 8, v1
	v_ashrrev_i32_e32 v3, 31, v2
	s_nop 15
	s_nop 15
	v_lshl_add_u64 v[8:9], v[2:3], 2, s[14:15]
	global_load_dword v248, v[8:9], off
	global_load_dword v249, v[8:9], off offset:64
	global_load_dword v250, v[8:9], off offset:128
	global_load_dword v251, v[8:9], off offset:192
	global_load_dword v252, v[8:9], off offset:512
	global_load_dword v253, v[8:9], off offset:576
	global_load_dword v254, v[8:9], off offset:640
	global_load_dword v255, v[8:9], off offset:704
	v_mov_b32_e32 v4, v154
	v_mov_b32_e32 v6, v150
	v_mov_b32_e32 v20, v151
	v_mov_b32_e32 v24, v152
	v_mov_b32_e32 v28, 0
	v_mov_b32_e32 v29, 0
	v_mov_b32_e32 v26, v153
	v_or_b32_e32 v32, 16, v2
	v_ashrrev_i32_e32 v33, 31, v32
	s_andn2_b64 vcc, exec, s[4:5]
	s_mov_b64 s[4:5], -1
	s_waitcnt vmcnt(7)
	v_mov_b32_e32 v3, v248
	v_mul_f32_e32 v10, 0x3d000000, v3
	v_mul_f32_e32 v11, v158, v10
	v_mul_f32_e32 v3, 0xbfb8aa3b, v11
	v_exp_f32_e32 v3, v3
	s_nop 0
	v_add_f32_e32 v3, 1.0, v3
	v_rcp_f32_e32 v5, v3
	s_nop 0
	v_pk_mul_f32 v[12:13], v[4:5], v[10:11]
	v_mul_f32_e32 v11, v159, v10
	v_mul_f32_e32 v3, 0xbfb8aa3b, v11
	v_exp_f32_e32 v3, v3
	v_mov_b32_e32 v4, v155
	v_mul_f32_e32 v12, v12, v13
	v_add_f32_e32 v3, 1.0, v3
	v_rcp_f32_e32 v5, v3
	s_nop 0
	v_pk_mul_f32 v[14:15], v[4:5], v[10:11]
	v_mul_f32_e32 v11, v160, v10
	v_mul_f32_e32 v3, 0xbfb8aa3b, v11
	v_exp_f32_e32 v3, v3
	v_mov_b32_e32 v4, v156
	v_add_f32_e32 v3, 1.0, v3
	v_rcp_f32_e32 v5, v3
	s_nop 0
	v_pk_mul_f32 v[16:17], v[4:5], v[10:11]
	v_mul_f32_e32 v11, v161, v10
	v_mul_f32_e32 v3, 0xbfb8aa3b, v11
	v_exp_f32_e32 v3, v3
	v_mov_b32_e32 v4, v157
	v_add_f32_e32 v3, 1.0, v3
	v_rcp_f32_e32 v5, v3
	s_nop 0
	v_pk_mul_f32 v[18:19], v[4:5], v[10:11]
	v_mul_f32_e32 v11, v146, v10
	v_mul_f32_e32 v3, 0xbfb8aa3b, v11
	v_exp_f32_e32 v3, v3
	v_lshl_or_b32 v4, s48, 7, v189
	v_ashrrev_i32_e32 v5, 31, v4
	v_add_f32_e32 v3, 1.0, v3
	v_rcp_f32_e32 v7, v3
	s_nop 0
	v_pk_mul_f32 v[22:23], v[6:7], v[10:11]
	v_mul_f32_e32 v11, v147, v10
	v_mul_f32_e32 v3, 0xbfb8aa3b, v11
	v_exp_f32_e32 v3, v3
	v_mov_b64_e32 v[6:7], s[12:13]
	v_mad_i64_i32 v[30:31], s[64:65], v2, s71, v[6:7]
	v_add_f32_e32 v3, 1.0, v3
	v_rcp_f32_e32 v21, v3
	s_nop 0
	v_pk_mul_f32 v[20:21], v[20:21], v[10:11]
	v_mul_f32_e32 v11, v148, v10
	v_mul_f32_e32 v3, 0xbfb8aa3b, v11
	v_exp_f32_e32 v3, v3
	s_nop 0
	v_add_f32_e32 v3, 1.0, v3
	v_rcp_f32_e32 v25, v3
	v_mul_f32_e32 v3, v14, v15
	v_cvt_pk_fp8_f32 v28, v12, v3
	v_mul_f32_e32 v3, v16, v17
	v_pk_mul_f32 v[12:13], v[24:25], v[10:11]
	v_mul_f32_e32 v11, v149, v10
	v_mul_f32_e32 v14, 0xbfb8aa3b, v11
	v_exp_f32_e32 v14, v14
	v_mul_f32_e32 v15, v18, v19
	v_cvt_pk_fp8_f32 v28, v3, v15 op_sel:[0,0,1]
	v_mul_f32_e32 v3, v22, v23
	v_add_f32_e32 v14, 1.0, v14
	v_rcp_f32_e32 v27, v14
	v_mul_f32_e32 v14, v20, v21
	v_cvt_pk_fp8_f32 v29, v3, v14
	v_mul_f32_e32 v3, v12, v13
	v_pk_mul_f32 v[10:11], v[26:27], v[10:11]
	v_lshl_add_u64 v[12:13], v[32:33], 2, s[14:15]
	v_mul_f32_e32 v10, v10, v11
	v_cvt_pk_fp8_f32 v29, v3, v10 op_sel:[0,0,1]
	v_lshl_add_u64 v[10:11], v[30:31], 0, v[4:5]
	v_mov_b32_e32 v14, v139
	v_mov_b32_e32 v16, v140
	global_store_dwordx2 v[10:11], v[28:29], off
	v_mov_b32_e32 v12, v138
	v_mov_b32_e32 v18, v141
	v_mov_b32_e32 v20, v134
	v_mov_b32_e32 v22, v135
	v_mov_b32_e32 v24, v136
	v_mov_b32_e32 v28, 0
	v_mov_b32_e32 v29, 0
	v_mov_b32_e32 v26, v137
	v_or_b32_e32 v30, 32, v2
	v_mad_i64_i32 v[32:33], s[64:65], v32, s71, v[6:7]
	v_ashrrev_i32_e32 v31, 31, v30
	s_waitcnt vmcnt(7)
	v_mov_b32_e32 v3, v249
	v_mul_f32_e32 v10, 0x3d000000, v3
	v_mul_f32_e32 v11, v142, v10
	v_mul_f32_e32 v3, 0xbfb8aa3b, v11
	v_exp_f32_e32 v3, v3
	s_nop 0
	v_add_f32_e32 v3, 1.0, v3
	v_rcp_f32_e32 v13, v3
	s_nop 0
	v_pk_mul_f32 v[12:13], v[12:13], v[10:11]
	v_mul_f32_e32 v11, v143, v10
	v_mul_f32_e32 v3, 0xbfb8aa3b, v11
	v_exp_f32_e32 v3, v3
	v_mul_f32_e32 v12, v12, v13
	v_add_f32_e32 v3, 1.0, v3
	v_rcp_f32_e32 v15, v3
	s_nop 0
	v_pk_mul_f32 v[14:15], v[14:15], v[10:11]
	v_mul_f32_e32 v11, v144, v10
	v_mul_f32_e32 v3, 0xbfb8aa3b, v11
	v_exp_f32_e32 v3, v3
	s_nop 0
	v_add_f32_e32 v3, 1.0, v3
	v_rcp_f32_e32 v17, v3
	s_nop 0
	v_pk_mul_f32 v[16:17], v[16:17], v[10:11]
	v_mul_f32_e32 v11, v145, v10
	v_mul_f32_e32 v3, 0xbfb8aa3b, v11
	v_exp_f32_e32 v3, v3
	s_nop 0
	v_add_f32_e32 v3, 1.0, v3
	v_rcp_f32_e32 v19, v3
	s_nop 0
	v_pk_mul_f32 v[18:19], v[18:19], v[10:11]
	v_mul_f32_e32 v11, v130, v10
	v_mul_f32_e32 v3, 0xbfb8aa3b, v11
	v_exp_f32_e32 v3, v3
	s_nop 0
	v_add_f32_e32 v3, 1.0, v3
	v_rcp_f32_e32 v21, v3
	s_nop 0
	v_pk_mul_f32 v[20:21], v[20:21], v[10:11]
	v_mul_f32_e32 v11, v131, v10
	v_mul_f32_e32 v3, 0xbfb8aa3b, v11
	v_exp_f32_e32 v3, v3
	s_nop 0
	v_add_f32_e32 v3, 1.0, v3
	v_rcp_f32_e32 v23, v3
	s_nop 0
	v_pk_mul_f32 v[22:23], v[22:23], v[10:11]
	v_mul_f32_e32 v11, v132, v10
	v_mul_f32_e32 v3, 0xbfb8aa3b, v11
	v_exp_f32_e32 v3, v3
	s_nop 0
	v_add_f32_e32 v3, 1.0, v3
	v_rcp_f32_e32 v25, v3
	v_mul_f32_e32 v3, v14, v15
	v_cvt_pk_fp8_f32 v28, v12, v3
	v_mul_f32_e32 v3, v16, v17
	v_pk_mul_f32 v[12:13], v[24:25], v[10:11]
	v_mul_f32_e32 v11, v133, v10
	v_mul_f32_e32 v14, 0xbfb8aa3b, v11
	v_exp_f32_e32 v14, v14
	v_mul_f32_e32 v15, v18, v19
	v_cvt_pk_fp8_f32 v28, v3, v15 op_sel:[0,0,1]
	v_mul_f32_e32 v3, v20, v21
	v_add_f32_e32 v14, 1.0, v14
	v_rcp_f32_e32 v27, v14
	v_mul_f32_e32 v14, v22, v23
	v_cvt_pk_fp8_f32 v29, v3, v14
	v_mul_f32_e32 v3, v12, v13
	v_pk_mul_f32 v[10:11], v[26:27], v[10:11]
	v_lshl_add_u64 v[12:13], v[30:31], 2, s[14:15]
	v_mul_f32_e32 v10, v10, v11
	v_cvt_pk_fp8_f32 v29, v3, v10 op_sel:[0,0,1]
	v_lshl_add_u64 v[10:11], v[32:33], 0, v[4:5]
	v_mov_b32_e32 v14, v123
	v_mov_b32_e32 v16, v124
	global_store_dwordx2 v[10:11], v[28:29], off
	v_mov_b32_e32 v12, v122
	v_mov_b32_e32 v18, v125
	v_mov_b32_e32 v20, v118
	v_mov_b32_e32 v22, v119
	v_mov_b32_e32 v24, v120
	v_mov_b32_e32 v28, 0
	v_mov_b32_e32 v29, 0
	v_mov_b32_e32 v26, v121
	v_or_b32_e32 v32, 48, v2
	v_mad_i64_i32 v[30:31], s[64:65], v30, s71, v[6:7]
	v_ashrrev_i32_e32 v33, 31, v32
	s_waitcnt vmcnt(7)
; __device__ __forceinline__ float sigm(float x) { return __builtin_amdgcn_rcpf(1.f + __builtin_amdgcn_exp2f(-1.4426950408889634f * x)); }
; __device__ __forceinline__ unsigned pk4_fp8(float a, float b, float c, float d) { int w = 0; w = __builtin_amdgcn_cvt_pk_fp8_f32(a, b, w, false); w = __builtin_amdgcn_cvt_pk_fp8_f32(c, d, w, true); return (unsigned)w; }
; __device__ __forceinline__ u32x4 pack8(f32x4 v0, f32x4 v1) { u32x4 w; w.x = cvt_pk_bf16(v0[0], v0[1]); w.y = cvt_pk_bf16(v0[2], v0[3]); w.z = cvt_pk_bf16(v1[0], v1[1]); w.w = cvt_pk_bf16(v1[2], v1[3]); return w; }
; template <class T> __device__ __forceinline__ void est(T* p, T v) { if constexpr (MK_EPI_NT != 0) __builtin_nontemporal_store(v, p); else *p = v; }
; __device__ __forceinline__ float ss_val(const ss_t* ss, int row) { return (float)ss[row] * (1.f / 16777216.f); }
;     __device__ __forceinline__ void operator()(AccT acc, const Unit& u, int wr, int wc, int fr, int fq) const {
;         const int row0 = u.pm * 256 + wr * 64 + fr, col0 = u.pn * 128 + wc * 32 + 8 * fq;
; #pragma unroll
;         for (int ai = 0; ai < 2; ++ai)
; #pragma unroll
;             for (int m = 0; m < 4; ++m) { const int row = row0 + ai * 128 + m * 16; const float r = (is_rstd ? ((const float*)rs)[row] : rsqrtf(ss_val((const ss_t*)rs, row) * (1.0f / DM) + EPS)) * ascale;
;                 f32x4 o[2];
; #pragma unroll
;                 for (int bj = 0; bj < 2; ++bj) { const f32x4 a = acc[ai][bj][m][0] * r, b = acc[ai][bj][m][1] * r;
; #pragma unroll
;                     for (int j = 0; j < 4; ++j) o[bj][j] = a[j] * sigm(a[j]) * b[j]; }
;                 if constexpr (F8OUT) est((u32x2*)((unsigned char*)O + (size_t)row * ldo + col0), (u32x2)(u32x2){pk4_fp8(o[0][0], o[0][1], o[0][2], o[0][3]), pk4_fp8(o[1][0], o[1][1], o[1][2], o[1][3])});
;                 else est((u32x4*)((bf16_t*)O + (size_t)row * ldo + col0), (u32x4)pack8(o[0], o[1])); }
;     }
	v_mov_b32_e32 v3, v250
	v_mul_f32_e32 v10, 0x3d000000, v3
	v_mul_f32_e32 v11, v126, v10
	v_mul_f32_e32 v3, 0xbfb8aa3b, v11
	v_exp_f32_e32 v3, v3
	s_nop 0
	v_add_f32_e32 v3, 1.0, v3
	v_rcp_f32_e32 v13, v3
	s_nop 0
	v_pk_mul_f32 v[12:13], v[12:13], v[10:11]
	v_mul_f32_e32 v11, v127, v10
	v_mul_f32_e32 v3, 0xbfb8aa3b, v11
	v_exp_f32_e32 v3, v3
	v_mul_f32_e32 v12, v12, v13
	v_add_f32_e32 v3, 1.0, v3
	v_rcp_f32_e32 v15, v3
	s_nop 0
	v_pk_mul_f32 v[14:15], v[14:15], v[10:11]
	v_mul_f32_e32 v11, v128, v10
	v_mul_f32_e32 v3, 0xbfb8aa3b, v11
	v_exp_f32_e32 v3, v3
	s_nop 0
	v_add_f32_e32 v3, 1.0, v3
	v_rcp_f32_e32 v17, v3
	s_nop 0
	v_pk_mul_f32 v[16:17], v[16:17], v[10:11]
	v_mul_f32_e32 v11, v129, v10
	v_mul_f32_e32 v3, 0xbfb8aa3b, v11
	v_exp_f32_e32 v3, v3
	s_nop 0
	v_add_f32_e32 v3, 1.0, v3
	v_rcp_f32_e32 v19, v3
	s_nop 0
	v_pk_mul_f32 v[18:19], v[18:19], v[10:11]
	v_mul_f32_e32 v11, v114, v10
	v_mul_f32_e32 v3, 0xbfb8aa3b, v11
	v_exp_f32_e32 v3, v3
	s_nop 0
	v_add_f32_e32 v3, 1.0, v3
	v_rcp_f32_e32 v21, v3
	s_nop 0
	v_pk_mul_f32 v[20:21], v[20:21], v[10:11]
	v_mul_f32_e32 v11, v115, v10
	v_mul_f32_e32 v3, 0xbfb8aa3b, v11
	v_exp_f32_e32 v3, v3
	s_nop 0
	v_add_f32_e32 v3, 1.0, v3
	v_rcp_f32_e32 v23, v3
	s_nop 0
	v_pk_mul_f32 v[22:23], v[22:23], v[10:11]
	v_mul_f32_e32 v11, v116, v10
	v_mul_f32_e32 v3, 0xbfb8aa3b, v11
	v_exp_f32_e32 v3, v3
	s_nop 0
	v_add_f32_e32 v3, 1.0, v3
	v_rcp_f32_e32 v25, v3
	v_mul_f32_e32 v3, v14, v15
	v_cvt_pk_fp8_f32 v28, v12, v3
	v_mul_f32_e32 v3, v16, v17
	v_pk_mul_f32 v[12:13], v[24:25], v[10:11]
	v_mul_f32_e32 v11, v117, v10
	v_mul_f32_e32 v14, 0xbfb8aa3b, v11
	v_exp_f32_e32 v14, v14
	v_mul_f32_e32 v15, v18, v19
	v_cvt_pk_fp8_f32 v28, v3, v15 op_sel:[0,0,1]
	v_mul_f32_e32 v3, v20, v21
	v_add_f32_e32 v14, 1.0, v14
	v_rcp_f32_e32 v27, v14
	v_mul_f32_e32 v14, v22, v23
	v_cvt_pk_fp8_f32 v29, v3, v14
	v_mul_f32_e32 v3, v12, v13
	v_pk_mul_f32 v[10:11], v[26:27], v[10:11]
	v_lshl_add_u64 v[12:13], v[32:33], 2, s[14:15]
	v_mul_f32_e32 v10, v10, v11
	v_cvt_pk_fp8_f32 v29, v3, v10 op_sel:[0,0,1]
	v_lshl_add_u64 v[10:11], v[30:31], 0, v[4:5]
	v_mov_b32_e32 v14, v107
	v_mov_b32_e32 v16, v108
	global_store_dwordx2 v[10:11], v[28:29], off
	v_mov_b32_e32 v12, v106
	v_mov_b32_e32 v18, v109
	v_mov_b32_e32 v20, v102
	v_mov_b32_e32 v22, v103
	v_mov_b32_e32 v24, v104
	v_mov_b32_e32 v28, 0
	v_mov_b32_e32 v29, 0
	v_mov_b32_e32 v26, v105
	v_add_u32_e32 v30, 0x80, v2
	s_waitcnt vmcnt(7)
	v_mov_b32_e32 v3, v251
	v_mul_f32_e32 v10, 0x3d000000, v3
	v_mul_f32_e32 v11, v110, v10
	v_mul_f32_e32 v3, 0xbfb8aa3b, v11
	v_exp_f32_e32 v3, v3
	s_nop 0
	v_add_f32_e32 v3, 1.0, v3
	v_rcp_f32_e32 v13, v3
	s_nop 0
	v_pk_mul_f32 v[12:13], v[12:13], v[10:11]
	v_mul_f32_e32 v11, v111, v10
	v_mul_f32_e32 v3, 0xbfb8aa3b, v11
	v_exp_f32_e32 v3, v3
	v_mul_f32_e32 v12, v12, v13
	v_add_f32_e32 v3, 1.0, v3
	v_rcp_f32_e32 v15, v3
	s_nop 0
	v_pk_mul_f32 v[14:15], v[14:15], v[10:11]
	v_mul_f32_e32 v11, v112, v10
	v_mul_f32_e32 v3, 0xbfb8aa3b, v11
	v_exp_f32_e32 v3, v3
	s_nop 0
	v_add_f32_e32 v3, 1.0, v3
	v_rcp_f32_e32 v17, v3
	s_nop 0
	v_pk_mul_f32 v[16:17], v[16:17], v[10:11]
	v_mul_f32_e32 v11, v113, v10
	v_mul_f32_e32 v3, 0xbfb8aa3b, v11
	v_exp_f32_e32 v3, v3
	s_nop 0
	v_add_f32_e32 v3, 1.0, v3
	v_rcp_f32_e32 v19, v3
	s_nop 0
	v_pk_mul_f32 v[18:19], v[18:19], v[10:11]
	v_mul_f32_e32 v11, v98, v10
	v_mul_f32_e32 v3, 0xbfb8aa3b, v11
	v_exp_f32_e32 v3, v3
	s_nop 0
	v_add_f32_e32 v3, 1.0, v3
	v_rcp_f32_e32 v21, v3
	s_nop 0
	v_pk_mul_f32 v[20:21], v[20:21], v[10:11]
	v_mul_f32_e32 v11, v99, v10
	v_mul_f32_e32 v3, 0xbfb8aa3b, v11
	v_exp_f32_e32 v3, v3
	s_nop 0
	v_add_f32_e32 v3, 1.0, v3
	v_rcp_f32_e32 v23, v3
	s_nop 0
	v_pk_mul_f32 v[22:23], v[22:23], v[10:11]
	v_mul_f32_e32 v11, v100, v10
	v_mul_f32_e32 v3, 0xbfb8aa3b, v11
	v_exp_f32_e32 v3, v3
	s_nop 0
	v_add_f32_e32 v3, 1.0, v3
	v_rcp_f32_e32 v25, v3
	v_mul_f32_e32 v3, v14, v15
	v_cvt_pk_fp8_f32 v28, v12, v3
	v_mul_f32_e32 v3, v16, v17
	v_pk_mul_f32 v[12:13], v[24:25], v[10:11]
	v_mul_f32_e32 v11, v101, v10
	v_mul_f32_e32 v14, 0xbfb8aa3b, v11
	v_exp_f32_e32 v14, v14
	v_mul_f32_e32 v15, v18, v19
	v_cvt_pk_fp8_f32 v28, v3, v15 op_sel:[0,0,1]
	v_mul_f32_e32 v3, v20, v21
	v_add_f32_e32 v14, 1.0, v14
	v_rcp_f32_e32 v27, v14
	v_mul_f32_e32 v14, v22, v23
	v_cvt_pk_fp8_f32 v29, v3, v14
	v_mul_f32_e32 v3, v12, v13
	v_pk_mul_f32 v[10:11], v[26:27], v[10:11]
	v_mov_b32_e32 v12, v90
	v_mul_f32_e32 v10, v10, v11
	v_cvt_pk_fp8_f32 v29, v3, v10 op_sel:[0,0,1]
	v_mad_i64_i32 v[10:11], s[64:65], v32, s71, v[6:7]
	v_lshl_add_u64 v[10:11], v[10:11], 0, v[4:5]
	global_store_dwordx2 v[10:11], v[28:29], off
	v_mov_b32_e32 v14, v91
	v_mov_b32_e32 v16, v92
	v_mov_b32_e32 v18, v93
	v_mov_b32_e32 v20, v86
	v_mov_b32_e32 v22, v87
	v_mov_b32_e32 v24, v88
	v_mov_b32_e32 v28, 0
	v_mov_b32_e32 v29, 0
	v_mov_b32_e32 v26, v89
	s_waitcnt vmcnt(7)
; __device__ __forceinline__ float sigm(float x) { return __builtin_amdgcn_rcpf(1.f + __builtin_amdgcn_exp2f(-1.4426950408889634f * x)); }
; __device__ __forceinline__ unsigned pk4_fp8(float a, float b, float c, float d) { int w = 0; w = __builtin_amdgcn_cvt_pk_fp8_f32(a, b, w, false); w = __builtin_amdgcn_cvt_pk_fp8_f32(c, d, w, true); return (unsigned)w; }
; __device__ __forceinline__ u32x4 pack8(f32x4 v0, f32x4 v1) { u32x4 w; w.x = cvt_pk_bf16(v0[0], v0[1]); w.y = cvt_pk_bf16(v0[2], v0[3]); w.z = cvt_pk_bf16(v1[0], v1[1]); w.w = cvt_pk_bf16(v1[2], v1[3]); return w; }
; template <class T> __device__ __forceinline__ void est(T* p, T v) { if constexpr (MK_EPI_NT != 0) __builtin_nontemporal_store(v, p); else *p = v; }
; __device__ __forceinline__ float ss_val(const ss_t* ss, int row) { return (float)ss[row] * (1.f / 16777216.f); }
;     __device__ __forceinline__ void operator()(AccT acc, const Unit& u, int wr, int wc, int fr, int fq) const {
;         const int row0 = u.pm * 256 + wr * 64 + fr, col0 = u.pn * 128 + wc * 32 + 8 * fq;
; #pragma unroll
;         for (int ai = 0; ai < 2; ++ai)
; #pragma unroll
;             for (int m = 0; m < 4; ++m) { const int row = row0 + ai * 128 + m * 16; const float r = (is_rstd ? ((const float*)rs)[row] : rsqrtf(ss_val((const ss_t*)rs, row) * (1.0f / DM) + EPS)) * ascale;
;                 f32x4 o[2];
; #pragma unroll
;                 for (int bj = 0; bj < 2; ++bj) { const f32x4 a = acc[ai][bj][m][0] * r, b = acc[ai][bj][m][1] * r;
; #pragma unroll
;                     for (int j = 0; j < 4; ++j) o[bj][j] = a[j] * sigm(a[j]) * b[j]; }
;                 if constexpr (F8OUT) est((u32x2*)((unsigned char*)O + (size_t)row * ldo + col0), (u32x2)(u32x2){pk4_fp8(o[0][0], o[0][1], o[0][2], o[0][3]), pk4_fp8(o[1][0], o[1][1], o[1][2], o[1][3])});
;                 else est((u32x4*)((bf16_t*)O + (size_t)row * ldo + col0), (u32x4)pack8(o[0], o[1])); }
;     }
	v_mov_b32_e32 v3, v252
	v_mul_f32_e32 v10, 0x3d000000, v3
	v_mul_f32_e32 v11, v94, v10
	v_mul_f32_e32 v3, 0xbfb8aa3b, v11
	v_exp_f32_e32 v3, v3
	s_nop 0
	v_add_f32_e32 v3, 1.0, v3
	v_rcp_f32_e32 v13, v3
	s_nop 0
	v_pk_mul_f32 v[12:13], v[12:13], v[10:11]
	v_mul_f32_e32 v11, v95, v10
	v_mul_f32_e32 v3, 0xbfb8aa3b, v11
	v_exp_f32_e32 v3, v3
	v_mul_f32_e32 v12, v12, v13
	v_add_f32_e32 v3, 1.0, v3
	v_rcp_f32_e32 v15, v3
	s_nop 0
	v_pk_mul_f32 v[14:15], v[14:15], v[10:11]
	v_mul_f32_e32 v11, v96, v10
	v_mul_f32_e32 v3, 0xbfb8aa3b, v11
	v_exp_f32_e32 v3, v3
	s_nop 0
	v_add_f32_e32 v3, 1.0, v3
	v_rcp_f32_e32 v17, v3
	s_nop 0
	v_pk_mul_f32 v[16:17], v[16:17], v[10:11]
	v_mul_f32_e32 v11, v97, v10
	v_mul_f32_e32 v3, 0xbfb8aa3b, v11
	v_exp_f32_e32 v3, v3
	s_nop 0
	v_add_f32_e32 v3, 1.0, v3
	v_rcp_f32_e32 v19, v3
	s_nop 0
	v_pk_mul_f32 v[18:19], v[18:19], v[10:11]
	v_mul_f32_e32 v11, v82, v10
	v_mul_f32_e32 v3, 0xbfb8aa3b, v11
	v_exp_f32_e32 v3, v3
	s_nop 0
	v_add_f32_e32 v3, 1.0, v3
	v_rcp_f32_e32 v21, v3
	s_nop 0
	v_pk_mul_f32 v[20:21], v[20:21], v[10:11]
	v_mul_f32_e32 v11, v83, v10
	v_mul_f32_e32 v3, 0xbfb8aa3b, v11
	v_exp_f32_e32 v3, v3
	s_nop 0
	v_add_f32_e32 v3, 1.0, v3
	v_rcp_f32_e32 v23, v3
	s_nop 0
	v_pk_mul_f32 v[22:23], v[22:23], v[10:11]
	v_mul_f32_e32 v11, v84, v10
	v_mul_f32_e32 v3, 0xbfb8aa3b, v11
	v_exp_f32_e32 v3, v3
	s_nop 0
	v_add_f32_e32 v3, 1.0, v3
	v_rcp_f32_e32 v25, v3
	v_mul_f32_e32 v3, v14, v15
	v_cvt_pk_fp8_f32 v28, v12, v3
	v_mul_f32_e32 v3, v16, v17
	v_pk_mul_f32 v[12:13], v[24:25], v[10:11]
	v_mul_f32_e32 v11, v85, v10
	v_mul_f32_e32 v14, 0xbfb8aa3b, v11
	v_exp_f32_e32 v14, v14
	v_mul_f32_e32 v15, v18, v19
	v_cvt_pk_fp8_f32 v28, v3, v15 op_sel:[0,0,1]
	v_mul_f32_e32 v3, v20, v21
	v_add_f32_e32 v14, 1.0, v14
	v_rcp_f32_e32 v27, v14
	v_mul_f32_e32 v14, v22, v23
	v_cvt_pk_fp8_f32 v29, v3, v14
	v_mul_f32_e32 v3, v12, v13
	v_pk_mul_f32 v[10:11], v[26:27], v[10:11]
	v_mov_b32_e32 v12, v74
	v_mul_f32_e32 v10, v10, v11
	v_cvt_pk_fp8_f32 v29, v3, v10 op_sel:[0,0,1]
	v_mad_i64_i32 v[10:11], s[64:65], v30, s71, v[6:7]
	v_lshl_add_u64 v[10:11], v[10:11], 0, v[4:5]
	global_store_dwordx2 v[10:11], v[28:29], off
	v_mov_b32_e32 v14, v75
	v_mov_b32_e32 v16, v76
	v_mov_b32_e32 v18, v77
	v_mov_b32_e32 v20, v70
	v_mov_b32_e32 v22, v71
	v_mov_b32_e32 v24, v72
	v_mov_b32_e32 v28, 0
	v_mov_b32_e32 v29, 0
	v_mov_b32_e32 v26, v73
	v_add_u32_e32 v30, 0x90, v2
	s_waitcnt vmcnt(7)
	v_mov_b32_e32 v3, v253
	v_mul_f32_e32 v10, 0x3d000000, v3
	v_mul_f32_e32 v11, v78, v10
	v_mul_f32_e32 v3, 0xbfb8aa3b, v11
	v_exp_f32_e32 v3, v3
	s_nop 0
	v_add_f32_e32 v3, 1.0, v3
	v_rcp_f32_e32 v13, v3
	s_nop 0
	v_pk_mul_f32 v[12:13], v[12:13], v[10:11]
	v_mul_f32_e32 v11, v79, v10
	v_mul_f32_e32 v3, 0xbfb8aa3b, v11
	v_exp_f32_e32 v3, v3
	v_mul_f32_e32 v12, v12, v13
	v_add_f32_e32 v3, 1.0, v3
	v_rcp_f32_e32 v15, v3
	s_nop 0
	v_pk_mul_f32 v[14:15], v[14:15], v[10:11]
	v_mul_f32_e32 v11, v80, v10
	v_mul_f32_e32 v3, 0xbfb8aa3b, v11
	v_exp_f32_e32 v3, v3
	s_nop 0
	v_add_f32_e32 v3, 1.0, v3
	v_rcp_f32_e32 v17, v3
	s_nop 0
	v_pk_mul_f32 v[16:17], v[16:17], v[10:11]
	v_mul_f32_e32 v11, v81, v10
	v_mul_f32_e32 v3, 0xbfb8aa3b, v11
	v_exp_f32_e32 v3, v3
	s_nop 0
	v_add_f32_e32 v3, 1.0, v3
	v_rcp_f32_e32 v19, v3
	s_nop 0
	v_pk_mul_f32 v[18:19], v[18:19], v[10:11]
	v_mul_f32_e32 v11, v66, v10
	v_mul_f32_e32 v3, 0xbfb8aa3b, v11
	v_exp_f32_e32 v3, v3
	s_nop 0
	v_add_f32_e32 v3, 1.0, v3
	v_rcp_f32_e32 v21, v3
	s_nop 0
	v_pk_mul_f32 v[20:21], v[20:21], v[10:11]
	v_mul_f32_e32 v11, v67, v10
	v_mul_f32_e32 v3, 0xbfb8aa3b, v11
	v_exp_f32_e32 v3, v3
	s_nop 0
	v_add_f32_e32 v3, 1.0, v3
	v_rcp_f32_e32 v23, v3
	s_nop 0
	v_pk_mul_f32 v[22:23], v[22:23], v[10:11]
	v_mul_f32_e32 v11, v68, v10
	v_mul_f32_e32 v3, 0xbfb8aa3b, v11
	v_exp_f32_e32 v3, v3
	s_nop 0
	v_add_f32_e32 v3, 1.0, v3
	v_rcp_f32_e32 v25, v3
	v_mul_f32_e32 v3, v14, v15
	v_cvt_pk_fp8_f32 v28, v12, v3
	v_mul_f32_e32 v3, v16, v17
	v_pk_mul_f32 v[12:13], v[24:25], v[10:11]
	v_mul_f32_e32 v11, v69, v10
	v_mul_f32_e32 v14, 0xbfb8aa3b, v11
	v_exp_f32_e32 v14, v14
	v_mul_f32_e32 v15, v18, v19
	v_cvt_pk_fp8_f32 v28, v3, v15 op_sel:[0,0,1]
	v_mul_f32_e32 v3, v20, v21
	v_add_f32_e32 v14, 1.0, v14
	v_rcp_f32_e32 v27, v14
	v_mul_f32_e32 v14, v22, v23
	v_cvt_pk_fp8_f32 v29, v3, v14
	v_mul_f32_e32 v3, v12, v13
	v_pk_mul_f32 v[10:11], v[26:27], v[10:11]
	v_mov_b32_e32 v12, v58
	v_mul_f32_e32 v10, v10, v11
	v_cvt_pk_fp8_f32 v29, v3, v10 op_sel:[0,0,1]
	v_mad_i64_i32 v[10:11], s[64:65], v30, s71, v[6:7]
	v_lshl_add_u64 v[10:11], v[10:11], 0, v[4:5]
	global_store_dwordx2 v[10:11], v[28:29], off
	v_mov_b32_e32 v14, v59
	v_mov_b32_e32 v16, v60
	v_mov_b32_e32 v18, v61
	v_mov_b32_e32 v20, v54
	v_mov_b32_e32 v22, v55
	v_mov_b32_e32 v24, v56
	v_mov_b32_e32 v28, 0
	v_mov_b32_e32 v29, 0
	v_mov_b32_e32 v26, v57
	v_add_u32_e32 v30, 0xa0, v2
	s_waitcnt vmcnt(7)
; __device__ __forceinline__ float sigm(float x) { return __builtin_amdgcn_rcpf(1.f + __builtin_amdgcn_exp2f(-1.4426950408889634f * x)); }
; __device__ __forceinline__ unsigned pk4_fp8(float a, float b, float c, float d) { int w = 0; w = __builtin_amdgcn_cvt_pk_fp8_f32(a, b, w, false); w = __builtin_amdgcn_cvt_pk_fp8_f32(c, d, w, true); return (unsigned)w; }
; __device__ __forceinline__ u32x4 pack8(f32x4 v0, f32x4 v1) { u32x4 w; w.x = cvt_pk_bf16(v0[0], v0[1]); w.y = cvt_pk_bf16(v0[2], v0[3]); w.z = cvt_pk_bf16(v1[0], v1[1]); w.w = cvt_pk_bf16(v1[2], v1[3]); return w; }
; template <class T> __device__ __forceinline__ void est(T* p, T v) { if constexpr (MK_EPI_NT != 0) __builtin_nontemporal_store(v, p); else *p = v; }
; __device__ __forceinline__ float ss_val(const ss_t* ss, int row) { return (float)ss[row] * (1.f / 16777216.f); }
;     ...
;         if constexpr (Epi::F8) asm volatile("s_nop 15\n\ts_nop 15" ::: "memory");
;         bool keep = false;
;         if constexpr (Epi::KEEP) keep = E(acc, cur, wr, wc, fr, fq); else E(acc, cur, wr, wc, fr, fq);
;     __device__ __forceinline__ void operator()(AccT acc, const Unit& u, int wr, int wc, int fr, int fq) const {
;         const int row0 = u.pm * 256 + wr * 64 + fr, col0 = u.pn * 128 + wc * 32 + 8 * fq;
; #pragma unroll
;         for (int ai = 0; ai < 2; ++ai)
; #pragma unroll
;             for (int m = 0; m < 4; ++m) { const int row = row0 + ai * 128 + m * 16; const float r = (is_rstd ? ((const float*)rs)[row] : rsqrtf(ss_val((const ss_t*)rs, row) * (1.0f / DM) + EPS)) * ascale;
;                 f32x4 o[2];
; #pragma unroll
;                 for (int bj = 0; bj < 2; ++bj) { const f32x4 a = acc[ai][bj][m][0] * r, b = acc[ai][bj][m][1] * r;
; #pragma unroll
;                     for (int j = 0; j < 4; ++j) o[bj][j] = a[j] * sigm(a[j]) * b[j]; }
;                 if constexpr (F8OUT) est((u32x2*)((unsigned char*)O + (size_t)row * ldo + col0), (u32x2)(u32x2){pk4_fp8(o[0][0], o[0][1], o[0][2], o[0][3]), pk4_fp8(o[1][0], o[1][1], o[1][2], o[1][3])});
;                 else est((u32x4*)((bf16_t*)O + (size_t)row * ldo + col0), (u32x4)pack8(o[0], o[1])); }
;     }
	v_mov_b32_e32 v3, v254
	v_mul_f32_e32 v10, 0x3d000000, v3
	v_mul_f32_e32 v11, v62, v10
	v_mul_f32_e32 v3, 0xbfb8aa3b, v11
	v_exp_f32_e32 v3, v3
	s_nop 0
	v_add_f32_e32 v3, 1.0, v3
	v_rcp_f32_e32 v13, v3
	s_nop 0
	v_pk_mul_f32 v[12:13], v[12:13], v[10:11]
	v_mul_f32_e32 v11, v63, v10
	v_mul_f32_e32 v3, 0xbfb8aa3b, v11
	v_exp_f32_e32 v3, v3
	v_mul_f32_e32 v12, v12, v13
	v_add_f32_e32 v3, 1.0, v3
	v_rcp_f32_e32 v15, v3
	s_nop 0
	v_pk_mul_f32 v[14:15], v[14:15], v[10:11]
	v_mul_f32_e32 v11, v64, v10
	v_mul_f32_e32 v3, 0xbfb8aa3b, v11
	v_exp_f32_e32 v3, v3
	s_nop 0
	v_add_f32_e32 v3, 1.0, v3
	v_rcp_f32_e32 v17, v3
	s_nop 0
	v_pk_mul_f32 v[16:17], v[16:17], v[10:11]
	v_mul_f32_e32 v11, v65, v10
	v_mul_f32_e32 v3, 0xbfb8aa3b, v11
	v_exp_f32_e32 v3, v3
	s_nop 0
	v_add_f32_e32 v3, 1.0, v3
	v_rcp_f32_e32 v19, v3
	s_nop 0
	v_pk_mul_f32 v[18:19], v[18:19], v[10:11]
	v_mul_f32_e32 v11, v50, v10
	v_mul_f32_e32 v3, 0xbfb8aa3b, v11
	v_exp_f32_e32 v3, v3
	s_nop 0
	v_add_f32_e32 v3, 1.0, v3
	v_rcp_f32_e32 v21, v3
	s_nop 0
	v_pk_mul_f32 v[20:21], v[20:21], v[10:11]
	v_mul_f32_e32 v11, v51, v10
	v_mul_f32_e32 v3, 0xbfb8aa3b, v11
	v_exp_f32_e32 v3, v3
	s_nop 0
	v_add_f32_e32 v3, 1.0, v3
	v_rcp_f32_e32 v23, v3
	s_nop 0
	v_pk_mul_f32 v[22:23], v[22:23], v[10:11]
	v_mul_f32_e32 v11, v52, v10
	v_mul_f32_e32 v3, 0xbfb8aa3b, v11
	v_exp_f32_e32 v3, v3
	s_nop 0
	v_add_f32_e32 v3, 1.0, v3
	v_rcp_f32_e32 v25, v3
	v_mul_f32_e32 v3, v14, v15
	v_cvt_pk_fp8_f32 v28, v12, v3
	v_mul_f32_e32 v3, v16, v17
	v_pk_mul_f32 v[12:13], v[24:25], v[10:11]
	v_mul_f32_e32 v11, v53, v10
	v_mul_f32_e32 v14, 0xbfb8aa3b, v11
	v_exp_f32_e32 v14, v14
	v_mul_f32_e32 v15, v18, v19
	v_cvt_pk_fp8_f32 v28, v3, v15 op_sel:[0,0,1]
	v_mul_f32_e32 v3, v20, v21
	v_add_f32_e32 v14, 1.0, v14
	v_rcp_f32_e32 v27, v14
	v_mul_f32_e32 v14, v22, v23
	v_cvt_pk_fp8_f32 v29, v3, v14
	v_mul_f32_e32 v3, v12, v13
	v_pk_mul_f32 v[10:11], v[26:27], v[10:11]
	v_mov_b32_e32 v12, v43
	v_mul_f32_e32 v10, v10, v11
	v_cvt_pk_fp8_f32 v29, v3, v10 op_sel:[0,0,1]
	v_mad_i64_i32 v[10:11], s[64:65], v30, s71, v[6:7]
	v_lshl_add_u64 v[10:11], v[10:11], 0, v[4:5]
	global_store_dwordx2 v[10:11], v[28:29], off
	v_mov_b32_e32 v10, v42
	v_mov_b32_e32 v14, v44
	v_mov_b32_e32 v16, v45
	v_mov_b32_e32 v18, v38
	v_mov_b32_e32 v20, v39
	v_mov_b32_e32 v22, v40
	v_mov_b32_e32 v26, 0
	v_add_u32_e32 v28, 0xb0, v2
	v_mov_b32_e32 v27, 0
	v_mov_b32_e32 v24, v41
	s_waitcnt vmcnt(7)
	v_mov_b32_e32 v3, v255
	v_mul_f32_e32 v8, 0x3d000000, v3
	v_mul_f32_e32 v9, v46, v8
	v_mul_f32_e32 v3, 0xbfb8aa3b, v9
	v_exp_f32_e32 v3, v3
	s_nop 0
	v_add_f32_e32 v3, 1.0, v3
	v_rcp_f32_e32 v11, v3
	s_nop 0
	v_pk_mul_f32 v[10:11], v[10:11], v[8:9]
	v_mul_f32_e32 v9, v47, v8
	v_mul_f32_e32 v3, 0xbfb8aa3b, v9
	v_exp_f32_e32 v3, v3
	v_mul_f32_e32 v2, v10, v11
	v_add_f32_e32 v3, 1.0, v3
	v_rcp_f32_e32 v13, v3
	s_nop 0
	v_pk_mul_f32 v[12:13], v[12:13], v[8:9]
	v_mul_f32_e32 v9, v48, v8
	v_mul_f32_e32 v3, 0xbfb8aa3b, v9
	v_exp_f32_e32 v3, v3
	s_nop 0
	v_add_f32_e32 v3, 1.0, v3
	v_rcp_f32_e32 v15, v3
	s_nop 0
	v_pk_mul_f32 v[14:15], v[14:15], v[8:9]
	v_mul_f32_e32 v9, v49, v8
	v_mul_f32_e32 v3, 0xbfb8aa3b, v9
	v_exp_f32_e32 v3, v3
	v_mul_f32_e32 v10, v14, v15
	v_add_f32_e32 v3, 1.0, v3
	v_rcp_f32_e32 v17, v3
	s_nop 0
	v_pk_mul_f32 v[16:17], v[16:17], v[8:9]
	v_mul_f32_e32 v9, v34, v8
	v_mul_f32_e32 v3, 0xbfb8aa3b, v9
	v_exp_f32_e32 v3, v3
	s_nop 0
	v_add_f32_e32 v3, 1.0, v3
	v_rcp_f32_e32 v19, v3
	s_nop 0
	v_pk_mul_f32 v[18:19], v[18:19], v[8:9]
	v_mul_f32_e32 v9, v35, v8
	v_mul_f32_e32 v3, 0xbfb8aa3b, v9
	v_exp_f32_e32 v3, v3
	s_nop 0
	v_add_f32_e32 v3, 1.0, v3
	v_rcp_f32_e32 v21, v3
	s_nop 0
	v_pk_mul_f32 v[20:21], v[20:21], v[8:9]
	v_mul_f32_e32 v9, v36, v8
	v_mul_f32_e32 v3, 0xbfb8aa3b, v9
	v_exp_f32_e32 v3, v3
	s_nop 0
	v_add_f32_e32 v3, 1.0, v3
	v_rcp_f32_e32 v23, v3
	v_mul_f32_e32 v3, v12, v13
	v_cvt_pk_fp8_f32 v26, v2, v3
	v_mul_f32_e32 v12, v16, v17
	v_pk_mul_f32 v[2:3], v[22:23], v[8:9]
	v_mul_f32_e32 v9, v37, v8
	v_mul_f32_e32 v11, 0xbfb8aa3b, v9
	v_exp_f32_e32 v11, v11
	v_cvt_pk_fp8_f32 v26, v10, v12 op_sel:[0,0,1]
	v_mul_f32_e32 v10, v18, v19
	v_add_f32_e32 v11, 1.0, v11
	v_rcp_f32_e32 v25, v11
	v_mul_f32_e32 v11, v20, v21
	v_cvt_pk_fp8_f32 v27, v10, v11
	v_mul_f32_e32 v10, v2, v3
	v_pk_mul_f32 v[2:3], v[24:25], v[8:9]
	s_nop 0
	v_mul_f32_e32 v2, v2, v3
	v_cvt_pk_fp8_f32 v27, v10, v2 op_sel:[0,0,1]
	v_mad_i64_i32 v[2:3], s[64:65], v28, s71, v[6:7]
	v_lshl_add_u64 v[2:3], v[2:3], 0, v[4:5]
	global_store_dwordx2 v[2:3], v[26:27], off
	s_cbranch_vccnz .LBB0_2254
	s_andn2_b64 vcc, exec, s[22:23]
	s_cbranch_vccnz .LBB0_2253
	s_barrier
	s_branch .LBB0_2253

; __global__ void __launch_bounds__(NWAVES * 64, 2) mk_fwd(Args a) {
	.amdhsa_kernel _Z6mk_fwd4Args
		.amdhsa_group_segment_fixed_size 0
		.amdhsa_private_segment_fixed_size 0
		.amdhsa_kernarg_size 528
		.amdhsa_user_sgpr_count 2
		.amdhsa_user_sgpr_dispatch_ptr 0
		.amdhsa_user_sgpr_queue_ptr 0
		.amdhsa_user_sgpr_kernarg_segment_ptr 1
		.amdhsa_user_sgpr_dispatch_id 0
		.amdhsa_user_sgpr_kernarg_preload_length 0
		.amdhsa_user_sgpr_kernarg_preload_offset 0
		.amdhsa_user_sgpr_private_segment_size 0
		.amdhsa_uses_dynamic_stack 0
		.amdhsa_enable_private_segment 0
		.amdhsa_system_sgpr_workgroup_id_x 1
		.amdhsa_system_sgpr_workgroup_id_y 0
		.amdhsa_system_sgpr_workgroup_id_z 0
		.amdhsa_system_sgpr_workgroup_info 0
		.amdhsa_system_vgpr_workitem_id 0
		.amdhsa_next_free_vgpr 256
		.amdhsa_next_free_sgpr 102
		.amdhsa_accum_offset 256
		.amdhsa_reserve_vcc 1
		.amdhsa_float_round_mode_32 0
		.amdhsa_float_round_mode_16_64 0
		.amdhsa_float_denorm_mode_32 3
		.amdhsa_float_denorm_mode_16_64 3
		.amdhsa_dx10_clamp 1
		.amdhsa_ieee_mode 1
		.amdhsa_fp16_overflow 0
		.amdhsa_tg_split 0
		.amdhsa_exception_fp_ieee_invalid_op 0
		.amdhsa_exception_fp_denorm_src 0
		.amdhsa_exception_fp_ieee_div_zero 0
		.amdhsa_exception_fp_ieee_overflow 0
		.amdhsa_exception_fp_ieee_underflow 0
		.amdhsa_exception_fp_ieee_inexact 0
		.amdhsa_exception_int_div_zero 0
	.end_amdhsa_kernel

; __global__ void __launch_bounds__(NWAVES * 64, 2) mk_fwd(Args a) {
amdhsa.kernels:
  - .agpr_count:     0
    .args:
      - .offset:         0
        .size:           272
        .value_kind:     by_value
      - .offset:         272
        .size:           4
        .value_kind:     hidden_block_count_x
      - .offset:         276
        .size:           4
        .value_kind:     hidden_block_count_y
      - .offset:         280
        .size:           4
        .value_kind:     hidden_block_count_z
      - .offset:         284
        .size:           2
        .value_kind:     hidden_group_size_x
      - .offset:         286
        .size:           2
        .value_kind:     hidden_group_size_y
      - .offset:         288
        .size:           2
        .value_kind:     hidden_group_size_z
      - .offset:         290
        .size:           2
        .value_kind:     hidden_remainder_x
      - .offset:         292
        .size:           2
        .value_kind:     hidden_remainder_y
      - .offset:         294
        .size:           2
        .value_kind:     hidden_remainder_z
      - .offset:         312
        .size:           8
        .value_kind:     hidden_global_offset_x
      - .offset:         320
        .size:           8
        .value_kind:     hidden_global_offset_y
      - .offset:         328
        .size:           8
        .value_kind:     hidden_global_offset_z
      - .offset:         336
        .size:           2
        .value_kind:     hidden_grid_dims
      - .offset:         392
        .size:           4
        .value_kind:     hidden_dynamic_lds_size
    .group_segment_fixed_size: 0
    .kernarg_segment_align: 8
    .kernarg_segment_size: 528
    .language:       OpenCL C
    .language_version:
      - 2
      - 0
    .max_flat_workgroup_size: 512
    .name:           _Z6mk_fwd4Args
    .private_segment_fixed_size: 0
    .sgpr_count:     108
    .sgpr_spill_count: 74
    .symbol:         _Z6mk_fwd4Args.kd
    .uniform_work_group_size: 1
    .uses_dynamic_stack: false
    .vgpr_count:     256
    .vgpr_spill_count: 0
    .wavefront_size: 64
